# xor-32 wave shuffles in MLA/stick-breaking tile loops via v_permlane32_swap instead of ds_bpermute LDS round trip
# baseline (speedup 1.0000x reference)
.LBB0_301:
	s_ashr_i32 s2, s72, 9
	s_lshl_b32 s3, s72, 8
	s_and_b32 s75, s3, 0x1f00
	s_ashr_i32 s3, s2, 31
	v_readlane_b32 s4, v239, 14
	s_bfe_u32 s43, s72, 0x40005
	s_lshl_b64 s[46:47], s[2:3], 13
	s_add_i32 s42, s75, s4
	s_mov_b64 s[40:41], s[78:79]
	v_mov_b32_e32 v34, v0
	s_add_u32 s4, s46, s42
	s_addc_u32 s5, s47, 0
	v_and_b32_e32 v19, 31, v34
	v_or_b32_e32 v82, s4, v19
	v_mov_b32_e32 v83, s5
	v_lshlrev_b64 v[2:3], 12, v[82:83]
	v_lshrrev_b32_e32 v5, 1, v34
	v_lshl_add_u64 v[2:3], s[0:1], 0, v[2:3]
	s_lshl_b32 s84, s43, 7
	v_lshl_add_u64 v[2:3], v[2:3], 0, s[84:85]
	v_and_b32_e32 v166, 16, v5
	v_add_u32_e32 v80, 0x600, v34
	v_lshl_add_u64 v[2:3], v[2:3], 0, v[166:167]
	s_addk_i32 s75, 0xff00
	v_ashrrev_i32_e32 v35, 3, v34
	v_ashrrev_i32_e32 v81, 3, v80
	global_load_dwordx4 v[50:53], v[2:3], off
	global_load_dwordx4 v[54:57], v[2:3], off offset:32
	global_load_dwordx4 v[58:61], v[2:3], off offset:64
	global_load_dwordx4 v[62:65], v[2:3], off offset:96
	v_add_u32_e32 v2, s75, v35
	v_add_u32_e32 v16, s75, v81
	v_max_i32_e32 v2, 0, v2
	v_mov_b32_e32 v3, v167
	v_max_i32_e32 v16, 0, v16
	v_mov_b32_e32 v17, v167
	v_lshl_add_u64 v[2:3], s[46:47], 0, v[2:3]
	v_lshl_add_u64 v[16:17], s[46:47], 0, v[16:17]
	v_lshlrev_b64 v[2:3], 12, v[2:3]
	v_lshlrev_b64 v[16:17], 12, v[16:17]
	v_lshlrev_b32_e32 v4, 2, v34
	v_lshl_add_u64 v[2:3], s[0:1], 0, v[2:3]
	v_lshlrev_b32_e32 v48, 4, v34
	v_lshl_add_u64 v[16:17], s[0:1], 0, v[16:17]
	v_and_b32_e32 v68, 12, v5
	v_and_b32_e32 v70, 16, v4
	v_lshl_add_u64 v[4:5], v[2:3], 0, s[84:85]
	v_and_b32_e32 v2, 0x70, v48
	v_mov_b32_e32 v3, v167
	v_lshl_add_u64 v[16:17], v[16:17], 0, s[84:85]
	s_waitcnt vmcnt(35)
	v_add_u32_e32 v88, 0x800, v34
	v_lshl_add_u64 v[16:17], v[16:17], 0, v[2:3]
	s_waitcnt vmcnt(19)
	v_ashrrev_i32_e32 v104, 3, v88
	global_load_dwordx4 v[20:23], v[16:17], off offset:2048
	v_add_u32_e32 v16, s75, v104
	v_max_i32_e32 v16, 0, v16
	v_mov_b32_e32 v17, v167
	v_lshl_add_u64 v[16:17], s[46:47], 0, v[16:17]
	v_lshlrev_b64 v[16:17], 12, v[16:17]
	v_lshl_add_u64 v[16:17], s[0:1], 0, v[16:17]
	v_lshl_add_u64 v[16:17], v[16:17], 0, s[84:85]
	v_add_u32_e32 v92, 0xa00, v34
	v_lshl_add_u64 v[16:17], v[16:17], 0, v[2:3]
	v_ashrrev_i32_e32 v105, 3, v92
	global_load_dwordx4 v[24:27], v[16:17], off offset:2048
	v_add_u32_e32 v16, s75, v105
	v_max_i32_e32 v16, 0, v16
	v_mov_b32_e32 v17, v167
	v_lshl_add_u64 v[16:17], s[46:47], 0, v[16:17]
	v_lshlrev_b64 v[16:17], 12, v[16:17]
	v_lshl_add_u64 v[16:17], s[0:1], 0, v[16:17]
	v_add_u32_e32 v49, 0x200, v34
	v_lshl_add_u64 v[16:17], v[16:17], 0, s[84:85]
	v_add_u32_e32 v96, 0xc00, v34
	v_ashrrev_i32_e32 v66, 3, v49
	v_lshl_add_u64 v[16:17], v[16:17], 0, v[2:3]
	v_ashrrev_i32_e32 v106, 3, v96
	v_add_u32_e32 v8, s75, v66
	global_load_dwordx4 v[28:31], v[16:17], off offset:2048
	v_add_u32_e32 v16, s75, v106
	v_max_i32_e32 v8, 0, v8
	v_mov_b32_e32 v9, v167
	v_add_u32_e32 v67, 0x400, v34
	v_max_i32_e32 v16, 0, v16
	v_mov_b32_e32 v17, v167
	v_lshl_add_u64 v[8:9], s[46:47], 0, v[8:9]
	v_ashrrev_i32_e32 v71, 3, v67
	v_lshl_add_u64 v[16:17], s[46:47], 0, v[16:17]
	v_lshl_add_u64 v[4:5], v[4:5], 0, v[2:3]
	v_lshlrev_b64 v[8:9], 12, v[8:9]
	v_add_u32_e32 v12, s75, v71
	v_lshlrev_b64 v[16:17], 12, v[16:17]
	global_load_dwordx4 v[4:7], v[4:5], off offset:2048
	v_lshl_add_u64 v[8:9], s[0:1], 0, v[8:9]
	v_max_i32_e32 v12, 0, v12
	v_mov_b32_e32 v13, v167
	v_lshl_add_u64 v[16:17], s[0:1], 0, v[16:17]
	v_lshl_add_u64 v[8:9], v[8:9], 0, s[84:85]
	v_lshl_add_u64 v[12:13], s[46:47], 0, v[12:13]
	v_lshl_add_u64 v[16:17], v[16:17], 0, s[84:85]
	v_add_u32_e32 v100, 0xe00, v34
	v_lshl_add_u64 v[8:9], v[8:9], 0, v[2:3]
	v_lshlrev_b64 v[12:13], 12, v[12:13]
	v_lshl_add_u64 v[16:17], v[16:17], 0, v[2:3]
	v_ashrrev_i32_e32 v107, 3, v100
	global_load_dwordx4 v[8:11], v[8:9], off offset:2048
	v_lshl_add_u64 v[12:13], s[0:1], 0, v[12:13]
	global_load_dwordx4 v[36:39], v[16:17], off offset:2048
	v_add_u32_e32 v16, s75, v107
	v_lshl_add_u64 v[12:13], v[12:13], 0, s[84:85]
	v_max_i32_e32 v16, 0, v16
	v_mov_b32_e32 v17, v167
	v_lshl_add_u64 v[12:13], v[12:13], 0, v[2:3]
	v_lshl_add_u64 v[16:17], s[46:47], 0, v[16:17]
	global_load_dwordx4 v[12:15], v[12:13], off offset:2048
	v_lshlrev_b64 v[16:17], 12, v[16:17]
	v_lshl_add_u64 v[16:17], s[0:1], 0, v[16:17]
	v_lshlrev_b32_e32 v32, 3, v34
	v_lshl_add_u64 v[16:17], v[16:17], 0, s[84:85]
	v_lshl_add_u64 v[16:17], v[16:17], 0, v[2:3]
	v_and_b32_e32 v3, 0x1f8, v32
	v_add_u32_e32 v3, s75, v3
	v_max_i32_e32 v3, 0, v3
	s_lshl_b32 s74, s43, 6
	global_load_dwordx4 v[40:43], v[16:17], off offset:2048
	s_lshl_b64 s[48:49], s[2:3], 14
	v_lshlrev_b32_e32 v16, 1, v3
	v_ashrrev_i32_e32 v3, 6, v34
	s_add_u32 s2, s67, s48
	v_add_u32_e32 v32, s74, v3
	s_addc_u32 s3, s68, s49
	v_mov_b32_e32 v17, v167
	v_ashrrev_i32_e32 v33, 31, v32
	v_lshl_add_u64 v[16:17], s[2:3], 0, v[16:17]
	v_lshlrev_b64 v[32:33], 15, v[32:33]
	v_lshl_add_u64 v[32:33], v[16:17], 0, v[32:33]
	v_ashrrev_i32_e32 v49, 6, v49
	global_load_dwordx4 v[44:47], v[32:33], off
	v_add_u32_e32 v32, s74, v49
	v_ashrrev_i32_e32 v33, 31, v32
	v_lshlrev_b64 v[32:33], 15, v[32:33]
	v_lshl_add_u64 v[32:33], v[16:17], 0, v[32:33]
	v_ashrrev_i32_e32 v67, 6, v67
	global_load_dwordx4 v[72:75], v[32:33], off
	v_add_u32_e32 v32, s74, v67
	v_ashrrev_i32_e32 v33, 31, v32
	v_lshlrev_b64 v[32:33], 15, v[32:33]
	v_lshl_add_u64 v[32:33], v[16:17], 0, v[32:33]
	v_ashrrev_i32_e32 v80, 6, v80
	global_load_dwordx4 v[76:79], v[32:33], off
	v_add_u32_e32 v32, s74, v80
	v_ashrrev_i32_e32 v33, 31, v32
	v_lshlrev_b64 v[32:33], 15, v[32:33]
	v_lshl_add_u64 v[32:33], v[16:17], 0, v[32:33]
	v_ashrrev_i32_e32 v108, 6, v88
	global_load_dwordx4 v[84:87], v[32:33], off
	v_add_u32_e32 v32, s74, v108
	v_ashrrev_i32_e32 v33, 31, v32
	v_lshlrev_b64 v[32:33], 15, v[32:33]
	v_lshl_add_u64 v[32:33], v[16:17], 0, v[32:33]
	v_ashrrev_i32_e32 v109, 6, v92
	global_load_dwordx4 v[88:91], v[32:33], off
	v_add_u32_e32 v32, s74, v109
	v_ashrrev_i32_e32 v33, 31, v32
	v_lshlrev_b64 v[32:33], 15, v[32:33]
	v_lshl_add_u64 v[32:33], v[16:17], 0, v[32:33]
	v_ashrrev_i32_e32 v110, 6, v96
	global_load_dwordx4 v[92:95], v[32:33], off
	v_add_u32_e32 v32, s74, v110
	v_ashrrev_i32_e32 v33, 31, v32
	v_lshlrev_b64 v[32:33], 15, v[32:33]
	v_lshl_add_u64 v[32:33], v[16:17], 0, v[32:33]
	global_load_dwordx4 v[96:99], v[32:33], off
	v_ashrrev_i32_e32 v111, 6, v100
	v_add_u32_e32 v32, s74, v111
	v_ashrrev_i32_e32 v33, 31, v32
	v_lshlrev_b64 v[32:33], 15, v[32:33]
	v_lshl_add_u64 v[16:17], v[16:17], 0, v[32:33]
	global_load_dwordx4 v[100:103], v[16:17], off
	s_movk_i32 s15, 0x90
	v_mul_lo_u32 v16, v35, s15
	v_add_u32_e32 v16, 0, v16
	v_and_b32_e32 v17, 16, v35
	v_add3_u32 v16, v16, v17, v2
	s_barrier
	s_waitcnt vmcnt(12)
	ds_write_b128 v16, v[4:7]
	v_mul_lo_u32 v4, v66, s15
	v_add_u32_e32 v4, 0, v4
	v_and_b32_e32 v5, 16, v66
	v_add3_u32 v4, v4, v5, v2
	s_waitcnt vmcnt(11)
	ds_write_b128 v4, v[8:11]
	v_mul_lo_u32 v4, v71, s15
	v_add_u32_e32 v4, 0, v4
	v_and_b32_e32 v5, 16, v71
	v_add3_u32 v4, v4, v5, v2
	s_waitcnt vmcnt(9)
	ds_write_b128 v4, v[12:15]
	v_mul_lo_u32 v4, v81, s15
	v_add_u32_e32 v4, 0, v4
	v_and_b32_e32 v5, 16, v81
	v_add3_u32 v4, v4, v5, v2
	ds_write_b128 v4, v[20:23]
	v_mul_lo_u32 v4, v104, s15
	v_add_u32_e32 v4, 0, v4
	v_and_b32_e32 v5, 16, v104
	v_add3_u32 v4, v4, v5, v2
	ds_write_b128 v4, v[24:27]
	v_mul_lo_u32 v4, v105, s15
	v_add_u32_e32 v4, 0, v4
	v_and_b32_e32 v5, 16, v105
	v_add3_u32 v4, v4, v5, v2
	ds_write_b128 v4, v[28:31]
	v_mul_lo_u32 v4, v106, s15
	v_add_u32_e32 v4, 0, v4
	v_and_b32_e32 v5, 16, v106
	v_add3_u32 v4, v4, v5, v2
	ds_write_b128 v4, v[36:39]
	v_mul_lo_u32 v4, v107, s15
	v_add_u32_e32 v4, 0, v4
	v_and_b32_e32 v5, 16, v107
	s_movk_i32 s2, 0x420
	v_add3_u32 v2, v4, v5, v2
	v_mul_lo_u32 v4, v3, s2
	s_add_i32 s36, 0, 0x12000
	s_waitcnt vmcnt(8)
	ds_write_b128 v2, v[40:43]
	v_and_b32_e32 v2, 0x3f0, v48
	v_add_u32_e32 v4, s36, v4
	v_and_b32_e32 v3, 16, v3
	v_add3_u32 v3, v4, v3, v2
	s_waitcnt vmcnt(7)
	ds_write_b128 v3, v[44:47]
	v_mul_lo_u32 v3, v49, s2
	v_add_u32_e32 v3, s36, v3
	v_and_b32_e32 v4, 16, v49
	v_add3_u32 v3, v3, v4, v2
	s_waitcnt vmcnt(6)
	ds_write_b128 v3, v[72:75]
	v_mul_lo_u32 v3, v67, s2
	v_add_u32_e32 v3, s36, v3
	v_and_b32_e32 v4, 16, v67
	v_add3_u32 v3, v3, v4, v2
	s_waitcnt vmcnt(5)
	ds_write_b128 v3, v[76:79]
	v_mul_lo_u32 v3, v80, s2
	v_add_u32_e32 v3, s36, v3
	v_and_b32_e32 v4, 16, v80
	v_add3_u32 v3, v3, v4, v2
	s_waitcnt vmcnt(4)
	ds_write_b128 v3, v[84:87]
	v_mul_lo_u32 v3, v108, s2
	v_add_u32_e32 v3, s36, v3
	v_and_b32_e32 v4, 16, v108
	v_add3_u32 v3, v3, v4, v2
	s_waitcnt vmcnt(3)
	ds_write_b128 v3, v[88:91]
	v_mul_lo_u32 v3, v109, s2
	v_add_u32_e32 v3, s36, v3
	v_and_b32_e32 v4, 16, v109
	v_add3_u32 v3, v3, v4, v2
	s_waitcnt vmcnt(2)
	ds_write_b128 v3, v[92:95]
	v_mul_lo_u32 v3, v110, s2
	v_add_u32_e32 v3, s36, v3
	v_and_b32_e32 v4, 16, v110
	s_cmp_gt_i32 s73, -1
	v_add3_u32 v3, v3, v4, v2
	s_cselect_b64 s[44:45], -1, 0
	s_waitcnt vmcnt(1)
	ds_write_b128 v3, v[96:99]
	v_mul_lo_u32 v3, v111, s2
	s_and_b64 s[2:3], s[44:45], exec
	s_cselect_b32 s4, s73, 0
	s_lshr_b32 s3, s4, 13
	s_lshr_b32 s2, s4, 8
	s_lshl_b32 s5, s3, 5
	s_sub_i32 s2, s2, s5
	s_cmp_eq_u32 s3, 1
	s_cselect_b32 s3, s63, s65
	s_cselect_b32 s5, s62, s64
	s_cmpk_lt_u32 s4, 0x2000
	s_cselect_b32 s3, s61, s3
	s_cselect_b32 s5, s60, s5
	s_add_u32 s6, s3, s70
	s_addc_u32 s5, s5, 0
	s_ashr_i32 s3, s2, 31
	s_lshl_b64 s[2:3], s[2:3], 22
	s_add_u32 s2, s6, s2
	s_addc_u32 s3, s5, s3
	s_lshl_b32 s5, s4, 2
	s_and_b32 s5, s5, 0x3c0
	v_readlane_b32 s6, v239, 17
	s_or_b32 s5, s5, s6
	s_lshl_b32 s5, s5, 12
	s_add_u32 s2, s2, s5
	s_addc_u32 s3, s3, 0
	s_lshl_b32 s4, s4, 8
	v_add_u32_e32 v3, s36, v3
	v_and_b32_e32 v4, 16, v111
	s_and_b32 s4, s4, 0xf00
	v_and_b32_e32 v1, 63, v34
	v_add3_u32 v2, v3, v4, v2
	s_add_u32 s2, s2, s4
	s_waitcnt vmcnt(0)
	ds_write_b128 v2, v[100:103]
	s_waitcnt lgkmcnt(0)
	s_barrier
	s_addc_u32 s3, s3, 0
	v_lshlrev_b32_e32 v2, 3, v1
	v_mov_b32_e32 v3, v167
	v_lshl_add_u64 v[4:5], s[2:3], 0, v[2:3]
	global_load_dwordx2 v[84:85], v2, s[2:3] nt
	s_movk_i32 s2, 0x2000
	v_add_co_u32_e32 v2, vcc, s2, v4
	s_movk_i32 s2, 0x6000
	s_nop 0
	v_addc_co_u32_e32 v3, vcc, 0, v5, vcc
	global_load_dwordx2 v[90:91], v[2:3], off offset:-4096 nt
	global_load_dwordx2 v[86:87], v[2:3], off nt
	v_add_co_u32_e32 v2, vcc, s77, v4
	v_readlane_b32 s7, v239, 18
	s_nop 0
	v_addc_co_u32_e32 v3, vcc, 0, v5, vcc
	global_load_dwordx2 v[96:97], v[2:3], off offset:-4096 nt
	global_load_dwordx2 v[88:89], v[2:3], off nt
	v_add_co_u32_e32 v2, vcc, s2, v4
	s_mov_b32 s2, 0xa000
	s_nop 0
	v_addc_co_u32_e32 v3, vcc, 0, v5, vcc
	global_load_dwordx2 v[106:107], v[2:3], off offset:-4096 nt
	global_load_dwordx2 v[100:101], v[2:3], off nt
	v_add_co_u32_e32 v2, vcc, s82, v4
	v_and_b32_e32 v69, 3, v34
	s_nop 0
	v_addc_co_u32_e32 v3, vcc, 0, v5, vcc
	global_load_dwordx2 v[102:103], v[2:3], off offset:-4096 nt
	global_load_dwordx2 v[92:93], v[2:3], off nt
	v_add_co_u32_e32 v2, vcc, s2, v4
	s_mov_b32 s2, 0xc000
	s_nop 0
	v_addc_co_u32_e32 v3, vcc, 0, v5, vcc
	global_load_dwordx2 v[118:119], v[2:3], off offset:-4096 nt
	global_load_dwordx2 v[108:109], v[2:3], off nt
	v_add_co_u32_e32 v2, vcc, s2, v4
	s_mov_b32 s2, 0xe000
	s_nop 0
	v_addc_co_u32_e32 v3, vcc, 0, v5, vcc
	global_load_dwordx2 v[110:111], v[2:3], off offset:-4096 nt
	global_load_dwordx2 v[94:95], v[2:3], off nt
	v_add_co_u32_e32 v2, vcc, s2, v4
	s_mov_b32 s2, 0x10000
	s_nop 0
	v_addc_co_u32_e32 v3, vcc, 0, v5, vcc
	global_load_dwordx2 v[126:127], v[2:3], off offset:-4096 nt
	global_load_dwordx2 v[112:113], v[2:3], off nt
	v_add_co_u32_e32 v2, vcc, s2, v4
	s_mov_b32 s2, 0x12000
	s_nop 0
	v_addc_co_u32_e32 v3, vcc, 0, v5, vcc
	global_load_dwordx2 v[120:121], v[2:3], off offset:-4096 nt
	global_load_dwordx2 v[98:99], v[2:3], off nt
	v_add_co_u32_e32 v2, vcc, s2, v4
	s_mov_b32 s2, 0x14000
	s_nop 0
	v_addc_co_u32_e32 v3, vcc, 0, v5, vcc
	global_load_dwordx2 v[128:129], v[2:3], off offset:-4096 nt
	global_load_dwordx2 v[114:115], v[2:3], off nt
	v_add_co_u32_e32 v2, vcc, s2, v4
	s_mov_b32 s2, 0x16000
	s_nop 0
	v_addc_co_u32_e32 v3, vcc, 0, v5, vcc
	global_load_dwordx2 v[122:123], v[2:3], off offset:-4096 nt
	global_load_dwordx2 v[104:105], v[2:3], off nt
	v_add_co_u32_e32 v2, vcc, s2, v4
	s_mov_b32 s2, 0x18000
	s_nop 0
	v_addc_co_u32_e32 v3, vcc, 0, v5, vcc
	global_load_dwordx2 v[134:135], v[2:3], off offset:-4096 nt
	global_load_dwordx2 v[130:131], v[2:3], off nt
	v_add_co_u32_e32 v2, vcc, s2, v4
	s_mov_b32 s2, 0x1a000
	s_nop 0
	v_addc_co_u32_e32 v3, vcc, 0, v5, vcc
	global_load_dwordx2 v[132:133], v[2:3], off offset:-4096 nt
	global_load_dwordx2 v[116:117], v[2:3], off nt
	v_add_co_u32_e32 v2, vcc, s2, v4
	s_mov_b32 s2, 0x1c000
	s_nop 0
	v_addc_co_u32_e32 v3, vcc, 0, v5, vcc
	global_load_dwordx2 v[142:143], v[2:3], off offset:-4096 nt
	global_load_dwordx2 v[136:137], v[2:3], off nt
	v_add_co_u32_e32 v2, vcc, s2, v4
	s_mov_b32 s2, 0x1e000
	s_nop 0
	v_addc_co_u32_e32 v3, vcc, 0, v5, vcc
	global_load_dwordx2 v[138:139], v[2:3], off offset:-4096 nt
	global_load_dwordx2 v[124:125], v[2:3], off nt
	v_add_co_u32_e32 v2, vcc, s2, v4
	s_mov_b32 s2, 0x1f000
	s_nop 0
	v_addc_co_u32_e32 v3, vcc, 0, v5, vcc
	global_load_dwordx2 v[144:145], v[2:3], off offset:-4096 nt
	global_load_dwordx2 v[140:141], v[2:3], off nt
	v_add_co_u32_e32 v2, vcc, s2, v4
	v_or3_b32 v18, v68, v69, v70
	s_nop 0
	v_addc_co_u32_e32 v3, vcc, 0, v5, vcc
	global_load_dwordx2 v[146:147], v[2:3], off nt
	v_or_b32_e32 v3, 1, v166
	v_cmp_lt_u32_e64 s[4:5], v3, v19
	v_or_b32_e32 v3, 2, v166
	v_cmp_lt_u32_e64 s[6:7], v3, v19
	v_or_b32_e32 v3, 3, v166
	v_cmp_lt_u32_e64 s[8:9], v3, v19
	v_or_b32_e32 v3, 4, v166
	v_cmp_lt_u32_e64 s[10:11], v3, v19
	v_or_b32_e32 v3, 5, v166
	v_readlane_b32 s14, v239, 15
	v_cmp_lt_u32_e64 s[12:13], v3, v19
	v_add_u32_e32 v2, 0, v70
	v_or_b32_e32 v3, s14, v18
	v_mul_lo_u32 v3, v3, s15
	v_add3_u32 v28, v2, v166, v3
	ds_read_b128 v[2:5], v28
	ds_read_b128 v[20:23], v28 offset:32
	v_or_b32_e32 v6, 6, v166
	v_cmp_lt_u32_e64 s[14:15], v6, v19
	v_or_b32_e32 v6, 7, v166
	v_cmp_lt_u32_e64 s[16:17], v6, v19
	v_or_b32_e32 v6, 8, v166
	v_cmp_lt_u32_e64 s[18:19], v6, v19
	s_waitcnt lgkmcnt(1)
	v_mfma_f32_32x32x16_bf16 v[2:17], v[2:5], v[50:53], 0
	v_or_b32_e32 v24, 9, v166
	v_cmp_lt_u32_e64 s[20:21], v24, v19
	v_or_b32_e32 v24, 10, v166
	v_cmp_lt_u32_e64 s[22:23], v24, v19
	v_or_b32_e32 v24, 11, v166
	v_cmp_lt_u32_e64 s[24:25], v24, v19
	ds_read_b128 v[24:27], v28 offset:64
	s_waitcnt lgkmcnt(1)
	v_mfma_f32_32x32x16_bf16 v[2:17], v[20:23], v[54:57], v[2:17]
	v_or_b32_e32 v20, 13, v166
	v_cmp_lt_u32_e64 s[28:29], v20, v19
	v_or_b32_e32 v20, 14, v166
	v_cmp_lt_u32_e64 s[30:31], v20, v19
	ds_read_b128 v[20:23], v28 offset:96
	v_or_b32_e32 v29, 12, v166
	v_cmp_lt_u32_e64 s[26:27], v29, v19
	s_waitcnt lgkmcnt(1)
	v_mfma_f32_32x32x16_bf16 v[2:17], v[24:27], v[58:61], v[2:17]
	v_and_b32_e32 v25, 64, v192
	v_xor_b32_e32 v24, 32, v192
	v_add_u32_e32 v25, 64, v25
	v_cmp_lt_i32_e32 vcc, v24, v25
	v_or_b32_e32 v29, 15, v166
	v_cmp_lt_u32_e64 s[34:35], v29, v19
	v_cndmask_b32_e32 v24, v192, v24, vcc
	s_waitcnt lgkmcnt(0)
	v_mfma_f32_32x32x16_bf16 v[2:17], v[20:23], v[62:65], v[2:17]
	v_lshlrev_b32_e32 v156, 2, v24
	v_cmp_lt_u32_e64 s[2:3], v166, v19
	v_and_b32_e32 v66, 32, v34
	v_mul_u32_u24_e32 v35, 0x420, v18
	s_mov_b64 s[50:51], -1
	s_nop 6
	v_pk_mul_f32 v[2:3], v[2:3], s[88:89] op_sel_hi:[1,0]
	s_nop 0
	v_min_f32_e32 v2, 0x42700000, v2
	v_pk_mul_f32 v[4:5], v[4:5], s[88:89] op_sel_hi:[1,0]
	v_exp_f32_e32 v22, v2
	v_min_f32_e32 v2, 0x42700000, v3
	v_exp_f32_e32 v23, v2
	v_min_f32_e32 v2, 0x42700000, v4
	v_pk_mul_f32 v[6:7], v[6:7], s[88:89] op_sel_hi:[1,0]
	v_exp_f32_e32 v24, v2
	v_min_f32_e32 v2, 0x42700000, v5
	v_exp_f32_e32 v25, v2
	v_min_f32_e32 v2, 0x42700000, v6
	v_pk_mul_f32 v[8:9], v[8:9], s[88:89] op_sel_hi:[1,0]
	v_exp_f32_e32 v6, v2
	v_min_f32_e32 v2, 0x42700000, v7
	v_exp_f32_e32 v7, v2
	v_min_f32_e32 v2, 0x42700000, v8
	v_pk_mul_f32 v[10:11], v[10:11], s[88:89] op_sel_hi:[1,0]
	v_exp_f32_e32 v8, v2
	v_min_f32_e32 v2, 0x42700000, v9
	v_exp_f32_e32 v9, v2
	v_min_f32_e32 v2, 0x42700000, v10
	v_pk_mul_f32 v[12:13], v[12:13], s[88:89] op_sel_hi:[1,0]
	v_exp_f32_e32 v10, v2
	v_min_f32_e32 v2, 0x42700000, v11
	v_exp_f32_e32 v11, v2
	v_min_f32_e32 v2, 0x42700000, v12
	v_pk_mul_f32 v[14:15], v[14:15], s[88:89] op_sel_hi:[1,0]
	v_exp_f32_e32 v12, v2
	v_min_f32_e32 v2, 0x42700000, v13
	v_exp_f32_e32 v13, v2
	v_min_f32_e32 v2, 0x42700000, v14
	v_pk_mul_f32 v[16:17], v[16:17], s[88:89] op_sel_hi:[1,0]
	v_exp_f32_e32 v26, v2
	v_min_f32_e32 v2, 0x42700000, v15
	v_min_f32_e32 v3, 0x42700000, v17
	v_exp_f32_e32 v27, v2
	v_min_f32_e32 v2, 0x42700000, v16
	v_exp_f32_e32 v14, v3
	v_exp_f32_e32 v40, v2
	v_add_f32_e32 v32, 1.0, v27
	v_add_f32_e32 v31, 1.0, v26
	v_add_f32_e32 v2, 1.0, v14
	v_add_f32_e32 v33, 1.0, v40
	v_rcp_f32_e32 v2, v2
	v_rcp_f32_e32 v33, v33
	v_rcp_f32_e32 v32, v32
	v_add_f32_e32 v30, 1.0, v13
	v_rcp_f32_e32 v31, v31
	v_add_f32_e32 v29, 1.0, v12
	v_rcp_f32_e32 v30, v30
	v_cndmask_b32_e64 v15, 1.0, v2, s[34:35]
	v_add_f32_e32 v28, 1.0, v11
	v_rcp_f32_e32 v29, v29
	v_cndmask_b32_e64 v33, 1.0, v33, s[30:31]
	v_add_f32_e32 v3, 1.0, v22
	v_add_f32_e32 v4, 1.0, v23
	v_add_f32_e32 v5, 1.0, v24
	v_add_f32_e32 v21, 1.0, v10
	v_rcp_f32_e32 v28, v28
	v_cndmask_b32_e64 v32, 1.0, v32, s[28:29]
	v_mul_f32_e32 v41, v33, v15
	v_rcp_f32_e32 v3, v3
	v_rcp_f32_e32 v4, v4
	v_rcp_f32_e32 v5, v5
	v_add_f32_e32 v20, 1.0, v9
	v_rcp_f32_e32 v21, v21
	v_cndmask_b32_e64 v31, 1.0, v31, s[26:27]
	v_mul_f32_e32 v32, v32, v41
	v_add_f32_e32 v19, 1.0, v8
	v_rcp_f32_e32 v20, v20
	v_cndmask_b32_e64 v30, 1.0, v30, s[24:25]
	v_mul_f32_e32 v31, v31, v32
	v_add_f32_e32 v17, 1.0, v7
	v_rcp_f32_e32 v19, v19
	v_cndmask_b32_e64 v29, 1.0, v29, s[22:23]
	v_mul_f32_e32 v30, v30, v31
	v_add_f32_e32 v16, 1.0, v6
	v_rcp_f32_e32 v17, v17
	v_cndmask_b32_e64 v28, 1.0, v28, s[20:21]
	v_mul_f32_e32 v29, v29, v30
	v_cndmask_b32_e64 v2, 1.0, v3, s[2:3]
	v_cndmask_b32_e64 v3, 1.0, v4, s[4:5]
	v_cndmask_b32_e64 v4, 1.0, v5, s[6:7]
	v_add_f32_e32 v5, 1.0, v25
	v_rcp_f32_e32 v16, v16
	v_cndmask_b32_e64 v21, 1.0, v21, s[18:19]
	v_mul_f32_e32 v28, v28, v29
	v_rcp_f32_e32 v5, v5
	v_cndmask_b32_e64 v20, 1.0, v20, s[16:17]
	v_mul_f32_e32 v33, v21, v28
	v_cndmask_b32_e64 v19, 1.0, v19, s[14:15]
	v_mul_f32_e32 v42, v20, v33
	v_cndmask_b32_e64 v17, 1.0, v17, s[12:13]
	v_mul_f32_e32 v43, v19, v42
	v_cndmask_b32_e64 v16, 1.0, v16, s[10:11]
	v_mul_f32_e32 v17, v17, v43
	v_cndmask_b32_e64 v5, 1.0, v5, s[8:9]
	v_mul_f32_e32 v16, v16, v17
	v_mul_f32_e32 v44, v5, v16
	v_mul_f32_e32 v45, v4, v44
	v_mul_f32_e32 v46, v3, v45
	v_mul_f32_e32 v47, v2, v46
	v_cmp_gt_u32_e64 s[100:101], 32, v1
	v_mov_b32_e32 v48, v47
	v_mov_b32_e32 v236, v47
	s_nop 1
	v_permlane32_swap_b32_e32 v48, v236
	v_cndmask_b32_e64 v48, v48, v236, s[100:101]
	v_add3_u32 v2, s36, v70, v66
	v_readlane_b32 s36, v239, 16
	s_waitcnt lgkmcnt(0)
	v_mul_f32_e32 v157, v47, v48
	v_add3_u32 v49, v2, s36, v35
	v_cmp_gt_u32_e64 s[36:37], 32, v1
	ds_read_b128 v[2:5], v49
	ds_read_b128 v[36:39], v49 offset:16
	ds_read_b128 v[18:21], v49 offset:33792
	v_cndmask_b32_e64 v48, 1.0, v48, s[36:37]
	v_mul_f32_e32 v16, v48, v16
	v_mul_f32_e32 v6, v6, v16
	v_mul_f32_e32 v16, v48, v17
	v_mul_f32_e32 v15, v48, v15
	v_mul_f32_e32 v7, v7, v16
	v_mul_f32_e32 v16, v48, v43
	v_mul_f32_e32 v14, v14, v15
	v_mul_f32_e32 v8, v8, v16
	v_mul_f32_e32 v16, v48, v42
	v_cndmask_b32_e64 v67, 0, v14, s[34:35]
	v_mul_f32_e32 v14, v48, v47
	v_mul_f32_e32 v9, v9, v16
	v_mul_f32_e32 v16, v48, v33
	v_mul_f32_e32 v14, v22, v14
	v_mul_f32_e32 v22, v48, v45
	v_mul_f32_e32 v10, v10, v16
	v_mul_f32_e32 v15, v48, v46
	v_mul_f32_e32 v22, v24, v22
	v_cndmask_b32_e64 v42, 0, v10, s[18:19]
	v_mul_f32_e32 v10, v48, v28
	v_mul_f32_e32 v15, v23, v15
	v_cndmask_b32_e64 v23, 0, v22, s[6:7]
	v_mul_f32_e32 v22, v48, v44
	v_mul_f32_e32 v10, v11, v10
	v_mul_f32_e32 v22, v25, v22
	v_cndmask_b32_e64 v43, 0, v10, s[20:21]
	v_mul_f32_e32 v10, v48, v29
	v_cndmask_b32_e64 v14, 0, v14, s[2:3]
	v_cndmask_b32_e64 v15, 0, v15, s[4:5]
	v_cndmask_b32_e64 v24, 0, v22, s[8:9]
	v_cndmask_b32_e64 v6, 0, v6, s[10:11]
	v_cndmask_b32_e64 v7, 0, v7, s[12:13]
	v_cndmask_b32_e64 v8, 0, v8, s[14:15]
	v_cndmask_b32_e64 v9, 0, v9, s[16:17]
	v_mul_f32_e32 v10, v12, v10
	v_cndmask_b32_e64 v44, 0, v10, s[22:23]
	v_mul_f32_e32 v10, v48, v30
	v_cvt_pk_bf16_f32 v22, v14, v15
	v_cvt_pk_bf16_f32 v23, v23, v24
	v_cvt_pk_bf16_f32 v24, v6, v7
	v_cvt_pk_bf16_f32 v25, v8, v9
	v_mul_f32_e32 v28, v13, v10
	v_cndmask_b32_e64 v45, 0, v28, s[24:25]
	s_waitcnt lgkmcnt(2)
	v_mfma_f32_32x32x16_bf16 v[2:17], v[2:5], v[22:25], 0
	v_mul_f32_e32 v28, v48, v31
	v_mul_f32_e32 v26, v26, v28
	v_cndmask_b32_e64 v46, 0, v26, s[26:27]
	v_mul_f32_e32 v26, v48, v32
	v_mul_f32_e32 v41, v48, v41
	v_mul_f32_e32 v26, v27, v26
	v_mul_f32_e32 v40, v40, v41
	v_cndmask_b32_e64 v47, 0, v26, s[28:29]
	v_cndmask_b32_e64 v48, 0, v40, s[30:31]
	v_cvt_pk_bf16_f32 v40, v42, v43
	v_cvt_pk_bf16_f32 v41, v44, v45
	v_cvt_pk_bf16_f32 v42, v46, v47
	v_cvt_pk_bf16_f32 v43, v48, v67
	s_waitcnt lgkmcnt(0)
	v_mfma_f32_32x32x16_bf16 v[18:33], v[18:21], v[22:25], 0
	v_cmp_eq_f32_e32 vcc, 0, v157
	s_cmp_eq_u64 vcc, exec
	v_mfma_f32_32x32x16_bf16 v[2:17], v[36:39], v[40:43], v[2:17]
	ds_read_b128 v[36:39], v49 offset:33808
	s_waitcnt lgkmcnt(0)
	v_mfma_f32_32x32x16_bf16 v[18:33], v[36:39], v[40:43], v[18:33]
	s_cbranch_scc1 .LBB0_307
	s_cmp_eq_u32 s42, 0
	s_cbranch_scc1 .LBB0_308
	v_bfe_u32 v36, v34, 2, 1
	v_bfe_u32 v34, v34, 3, 2
	v_mul_u32_u24_e32 v36, 0x910, v36
	v_mul_u32_u24_e32 v34, 0x240, v34
	v_readlane_b32 s52, v239, 39
	s_sub_i32 s42, s42, 32
	s_nop 0
	v_add3_u32 v34, s52, v36, v34
	v_mul_u32_u24_e32 v36, 0x90, v69
	v_readlane_b32 s52, v239, 51
	v_add3_u32 v67, v34, v36, v166
	s_nop 0
	v_add_u32_e32 v34, s52, v35
	v_add3_u32 v71, v34, v66, v70
	s_branch .LBB0_305

.LBB0_305:
	v_add_u32_e32 v76, 0, v67
	ds_read_b128 v[34:37], v76
	ds_read_b128 v[72:75], v76 offset:32
	v_add_u32_e32 v173, 0, v71
	v_add_u32_e32 v172, 0x121c0, v173
	v_add_u32_e32 v175, 0x121d0, v173
	s_waitcnt lgkmcnt(1)
	v_mfma_f32_32x32x16_bf16 v[34:49], v[34:37], v[50:53], 0
	s_mov_b64 s[54:55], -1
	s_waitcnt lgkmcnt(0)
	v_mfma_f32_32x32x16_bf16 v[34:49], v[72:75], v[54:57], v[34:49]
	ds_read_b128 v[72:75], v76 offset:64
	ds_read_b128 v[76:79], v76 offset:96
	s_waitcnt lgkmcnt(1)
	v_mfma_f32_32x32x16_bf16 v[34:49], v[72:75], v[58:61], v[34:49]
	s_waitcnt lgkmcnt(0)
	v_mfma_f32_32x32x16_bf16 v[34:49], v[76:79], v[62:65], v[34:49]
	s_nop 11
	v_pk_mul_f32 v[46:47], v[46:47], s[88:89] op_sel_hi:[1,0]
	v_pk_mul_f32 v[48:49], v[48:49], s[88:89] op_sel_hi:[1,0]
	v_min_f32_e32 v47, 0x42700000, v47
	v_pk_mul_f32 v[44:45], v[44:45], s[88:89] op_sel_hi:[1,0]
	v_exp_f32_e32 v151, v47
	v_min_f32_e32 v47, 0x42700000, v48
	v_min_f32_e32 v44, 0x42700000, v44
	v_exp_f32_e32 v152, v47
	v_min_f32_e32 v47, 0x42700000, v49
	v_exp_f32_e32 v148, v44
	v_min_f32_e32 v44, 0x42700000, v45
	v_exp_f32_e32 v153, v47
	v_exp_f32_e32 v149, v44
	v_min_f32_e32 v44, 0x42700000, v46
	v_pk_mul_f32 v[42:43], v[42:43], s[88:89] op_sel_hi:[1,0]
	v_exp_f32_e32 v150, v44
	v_min_f32_e32 v42, 0x42700000, v42
	v_exp_f32_e32 v80, v42
	v_min_f32_e32 v42, 0x42700000, v43
	v_add_f32_e32 v48, 1.0, v152
	v_add_f32_e32 v49, 1.0, v153
	v_pk_mul_f32 v[40:41], v[40:41], s[88:89] op_sel_hi:[1,0]
	v_exp_f32_e32 v81, v42
	v_add_f32_e32 v47, 1.0, v151
	v_rcp_f32_e32 v48, v48
	v_rcp_f32_e32 v155, v49
	v_min_f32_e32 v41, 0x42700000, v41
	v_add_f32_e32 v46, 1.0, v150
	v_rcp_f32_e32 v47, v47
	v_pk_mul_f32 v[38:39], v[38:39], s[88:89] op_sel_hi:[1,0]
	v_min_f32_e32 v40, 0x42700000, v40
	v_exp_f32_e32 v79, v41
	v_add_f32_e32 v45, 1.0, v149
	v_rcp_f32_e32 v46, v46
	v_min_f32_e32 v39, 0x42700000, v39
	v_exp_f32_e32 v78, v40
	v_add_f32_e32 v44, 1.0, v148
	v_rcp_f32_e32 v45, v45
	v_pk_mul_f32 v[36:37], v[36:37], s[88:89] op_sel_hi:[1,0]
	v_min_f32_e32 v38, 0x42700000, v38
	v_exp_f32_e32 v77, v39
	v_add_f32_e32 v43, 1.0, v81
	v_rcp_f32_e32 v44, v44
	v_mul_f32_e32 v154, v48, v155
	v_min_f32_e32 v37, 0x42700000, v37
	v_exp_f32_e32 v76, v38
	v_add_f32_e32 v42, 1.0, v80
	v_rcp_f32_e32 v43, v43
	v_mul_f32_e32 v159, v47, v154
	v_pk_mul_f32 v[34:35], v[34:35], s[88:89] op_sel_hi:[1,0]
	v_min_f32_e32 v36, 0x42700000, v36
	v_exp_f32_e32 v75, v37
	v_add_f32_e32 v41, 1.0, v79
	v_rcp_f32_e32 v42, v42
	v_mul_f32_e32 v158, v46, v159
	v_min_f32_e32 v35, 0x42700000, v35
	v_exp_f32_e32 v74, v36
	v_add_f32_e32 v40, 1.0, v78
	v_rcp_f32_e32 v41, v41
	v_mul_f32_e32 v161, v45, v158
	v_min_f32_e32 v34, 0x42700000, v34
	v_exp_f32_e32 v73, v35
	v_add_f32_e32 v39, 1.0, v77
	v_rcp_f32_e32 v40, v40
	v_mul_f32_e32 v160, v44, v161
	v_exp_f32_e32 v72, v34
	v_add_f32_e32 v38, 1.0, v76
	v_rcp_f32_e32 v39, v39
	v_mul_f32_e32 v163, v43, v160
	v_add_f32_e32 v37, 1.0, v75
	v_rcp_f32_e32 v38, v38
	v_mul_f32_e32 v162, v42, v163
	v_add_f32_e32 v36, 1.0, v74
	v_rcp_f32_e32 v37, v37
	v_mul_f32_e32 v43, v41, v162
	v_add_f32_e32 v35, 1.0, v73
	v_rcp_f32_e32 v36, v36
	v_mul_f32_e32 v42, v40, v43
	v_add_f32_e32 v34, 1.0, v72
	v_rcp_f32_e32 v35, v35
	v_mul_f32_e32 v45, v39, v42
	v_rcp_f32_e32 v34, v34
	v_mul_f32_e32 v44, v38, v45
	v_mul_f32_e32 v47, v37, v44
	v_mul_f32_e32 v46, v36, v47
	v_mul_f32_e32 v165, v35, v46
	v_mul_f32_e32 v164, v34, v165
	v_mov_b32_e32 v174, v164
	v_mov_b32_e32 v236, v164
	s_nop 1
	v_permlane32_swap_b32_e32 v174, v236
	v_cndmask_b32_e64 v174, v174, v236, s[36:37]
	ds_read_b128 v[34:37], v172
	v_add_u32_e32 v38, 0x1a5c0, v173
	ds_read_b128 v[38:41], v38
	s_waitcnt lgkmcnt(2)
	v_cndmask_b32_e64 v48, 1.0, v174, s[36:37]
	v_mul_f32_e32 v172, v157, v48
	v_pk_mul_f32 v[48:49], v[172:173], v[164:165] op_sel_hi:[0,1]
	v_pk_mul_f32 v[46:47], v[172:173], v[46:47] op_sel_hi:[0,1]
	v_pk_mul_f32 v[44:45], v[172:173], v[44:45] op_sel_hi:[0,1]
	v_pk_mul_f32 v[42:43], v[172:173], v[42:43] op_sel_hi:[0,1]
	v_pk_mul_f32 v[48:49], v[72:73], v[48:49]
	v_pk_mul_f32 v[46:47], v[74:75], v[46:47]
	v_pk_mul_f32 v[44:45], v[76:77], v[44:45]
	v_pk_mul_f32 v[72:73], v[78:79], v[42:43]
	v_cvt_pk_bf16_f32 v42, v48, v49
	v_cvt_pk_bf16_f32 v43, v46, v47
	v_cvt_pk_bf16_f32 v44, v44, v45
	v_cvt_pk_bf16_f32 v45, v72, v73
	ds_read_b128 v[46:49], v175
	v_pk_mul_f32 v[76:77], v[172:173], v[158:159] op_sel_hi:[0,1]
	s_waitcnt lgkmcnt(2)
	v_mfma_f32_32x32x16_bf16 v[2:17], v[34:37], v[42:45], v[2:17]
	v_mul_f32_e64 v34, v172, v162
	v_mul_f32_e64 v35, v172, v163
	v_add_u32_e32 v36, 0x1a5d0, v173
	v_mul_f32_e64 v72, v80, v34
	v_mul_f32_e64 v73, v81, v35
	v_pk_mul_f32 v[34:35], v[172:173], v[160:161] op_sel_hi:[0,1]
	v_pk_mul_f32 v[74:75], v[148:149], v[34:35]
	ds_read_b128 v[34:37], v36
	s_waitcnt lgkmcnt(2)
	v_mfma_f32_32x32x16_bf16 v[18:33], v[38:41], v[42:45], v[18:33]
	v_mul_f32_e64 v38, v172, v154
	v_mul_f32_e64 v39, v172, v155
	v_mul_f32_e64 v40, v150, v76
	v_mul_f32_e64 v41, v151, v77
	v_mul_f32_e64 v42, v152, v38
	v_mul_f32_e64 v43, v153, v39
	v_cvt_pk_bf16_f32 v38, v72, v73
	v_cvt_pk_bf16_f32 v39, v74, v75
	v_cvt_pk_bf16_f32 v40, v40, v41
	v_cvt_pk_bf16_f32 v41, v42, v43
	v_mul_f32_e32 v42, v164, v174
	v_mul_f32_e32 v157, v157, v42
	s_waitcnt lgkmcnt(1)
	v_mfma_f32_32x32x16_bf16 v[2:17], v[46:49], v[38:41], v[2:17]
	v_cmp_eq_f32_e32 vcc, 0, v157
	s_cmp_eq_u64 vcc, exec
	s_waitcnt lgkmcnt(0)
	v_mfma_f32_32x32x16_bf16 v[18:33], v[34:37], v[38:41], v[18:33]
	s_cbranch_scc0 .LBB0_304
	s_mov_b64 s[52:53], -1
	s_branch .LBB0_309

.LBB0_315:
	v_mul_f32_e32 v152, v152, v153
	v_mul_f32_e32 v175, v175, v152
	v_mul_f32_e32 v174, v174, v175
	v_mul_f32_e32 v173, v173, v174
	v_mul_f32_e32 v172, v172, v173
	v_mul_f32_e32 v165, v165, v172
	v_mul_f32_e32 v164, v164, v165
	v_mul_f32_e32 v163, v163, v164
	v_mul_f32_e32 v162, v162, v163
	v_mul_f32_e32 v161, v161, v162
	v_mul_f32_e32 v160, v160, v161
	v_mul_f32_e32 v177, v159, v160
	v_mul_f32_e32 v176, v158, v177
	v_mul_f32_e32 v155, v155, v176
	v_mul_f32_e32 v154, v154, v155
	v_mov_b32_e32 v158, v154
	v_mov_b32_e32 v236, v154
	s_nop 1
	v_permlane32_swap_b32_e32 v158, v236
	v_cndmask_b32_e64 v158, v158, v236, s[36:37]
	s_andn2_b64 vcc, exec, s[46:47]
	s_waitcnt lgkmcnt(0)
	v_cndmask_b32_e64 v159, 1.0, v158, s[36:37]
	v_mul_f32_e32 v178, v157, v159
	v_pk_mul_f32 v[160:161], v[178:179], v[160:161] op_sel_hi:[0,1]
	v_pk_mul_f32 v[48:49], v[48:49], v[160:161]
	v_pk_mul_f32 v[160:161], v[178:179], v[162:163] op_sel_hi:[0,1]
	v_pk_mul_f32 v[42:43], v[42:43], v[160:161]
	v_pk_mul_f32 v[160:161], v[178:179], v[164:165] op_sel_hi:[0,1]
	v_pk_mul_f32 v[40:41], v[40:41], v[160:161]
	v_pk_mul_f32 v[160:161], v[178:179], v[172:173] op_sel_hi:[0,1]
	v_pk_mul_f32 v[180:181], v[178:179], v[154:155] op_sel_hi:[0,1]
	v_pk_mul_f32 v[176:177], v[178:179], v[176:177] op_sel_hi:[0,1]
	v_pk_mul_f32 v[38:39], v[38:39], v[160:161]
	v_pk_mul_f32 v[160:161], v[174:175], v[178:179] op_sel_hi:[1,0]
	v_pk_mul_f32 v[152:153], v[152:153], v[178:179] op_sel_hi:[1,0]
	v_pk_mul_f32 v[44:45], v[44:45], v[180:181]
	v_pk_mul_f32 v[46:47], v[46:47], v[176:177]
	v_pk_mul_f32 v[36:37], v[36:37], v[160:161]
	v_pk_mul_f32 v[34:35], v[34:35], v[152:153]
	s_cbranch_vccnz .LBB0_317
	v_cndmask_b32_e64 v44, 0, v44, s[2:3]
	v_cndmask_b32_e64 v45, 0, v45, s[4:5]
	v_cndmask_b32_e64 v46, 0, v46, s[6:7]
	v_cndmask_b32_e64 v47, 0, v47, s[8:9]
	v_cndmask_b32_e64 v48, 0, v48, s[10:11]
	v_cndmask_b32_e64 v49, 0, v49, s[12:13]
	v_cndmask_b32_e64 v42, 0, v42, s[14:15]
	v_cndmask_b32_e64 v43, 0, v43, s[16:17]
	v_cndmask_b32_e64 v40, 0, v40, s[18:19]
	v_cndmask_b32_e64 v41, 0, v41, s[20:21]
	v_cndmask_b32_e64 v38, 0, v38, s[22:23]
	v_cndmask_b32_e64 v39, 0, v39, s[24:25]
	v_cndmask_b32_e64 v36, 0, v36, s[26:27]
	v_cndmask_b32_e64 v37, 0, v37, s[28:29]
	v_cndmask_b32_e64 v34, 0, v34, s[30:31]
	v_cndmask_b32_e64 v35, 0, v35, s[34:35]

.LBB0_463:
	s_nop 9
	v_max_f32_e32 v206, v82, v66
	v_max_f32_e32 v208, v83, v67
	v_max3_f32 v206, v206, s90, v208
	v_max_f32_e32 v208, v84, v68
	v_max_f32_e32 v209, v85, v69
	v_max3_f32 v206, v206, v208, v209
	v_max_f32_e32 v208, v86, v70
	v_max_f32_e32 v209, v87, v71
	v_max3_f32 v206, v206, v208, v209
	v_max_f32_e32 v208, v88, v72
	v_max_f32_e32 v209, v89, v73
	v_max3_f32 v206, v206, v208, v209
	v_max_f32_e32 v208, v90, v74
	v_max_f32_e32 v209, v91, v75
	v_max3_f32 v206, v206, v208, v209
	v_max_f32_e32 v208, v92, v76
	v_max_f32_e32 v209, v93, v77
	v_max3_f32 v206, v206, v208, v209
	v_max_f32_e32 v208, v94, v78
	v_max_f32_e32 v209, v95, v79
	v_max3_f32 v206, v206, v208, v209
	v_max_f32_e32 v208, v96, v80
	v_max_f32_e32 v209, v97, v81
	v_max3_f32 v206, v206, v208, v209
	v_mov_b32_e32 v208, v206
	v_mov_b32_e32 v209, v206
	s_nop 1
	v_permlane32_swap_b32_e32 v208, v209
	v_max3_f32 v206, v207, v208, v209
	v_cmp_neq_f32_e32 vcc, v206, v207
	s_cbranch_vccz .LBB0_465
	v_sub_f32_e32 v207, v207, v206
	v_mul_f32_e32 v207, 0x3dd53b94, v207
	v_exp_f32_e32 v208, v207
	s_nop 0
	v_pk_mul_f32 v[64:65], v[64:65], v[208:209] op_sel_hi:[1,0]
	v_pk_mul_f32 v[62:63], v[62:63], v[208:209] op_sel_hi:[1,0]
	v_pk_mul_f32 v[60:61], v[60:61], v[208:209] op_sel_hi:[1,0]
	v_pk_mul_f32 v[58:59], v[58:59], v[208:209] op_sel_hi:[1,0]
	v_pk_mul_f32 v[56:57], v[56:57], v[208:209] op_sel_hi:[1,0]
	v_pk_mul_f32 v[54:55], v[54:55], v[208:209] op_sel_hi:[1,0]
	v_pk_mul_f32 v[52:53], v[52:53], v[208:209] op_sel_hi:[1,0]
	v_pk_mul_f32 v[50:51], v[50:51], v[208:209] op_sel_hi:[1,0]
	v_pk_mul_f32 v[48:49], v[48:49], v[208:209] op_sel_hi:[1,0]
	v_pk_mul_f32 v[46:47], v[46:47], v[208:209] op_sel_hi:[1,0]
	v_pk_mul_f32 v[44:45], v[44:45], v[208:209] op_sel_hi:[1,0]
	v_pk_mul_f32 v[42:43], v[42:43], v[208:209] op_sel_hi:[1,0]
	v_pk_mul_f32 v[40:41], v[40:41], v[208:209] op_sel_hi:[1,0]
	v_pk_mul_f32 v[38:39], v[38:39], v[208:209] op_sel_hi:[1,0]
	v_pk_mul_f32 v[36:37], v[36:37], v[208:209] op_sel_hi:[1,0]
	v_pk_mul_f32 v[34:35], v[34:35], v[208:209] op_sel_hi:[1,0]
	v_pk_mul_f32 v[32:33], v[32:33], v[208:209] op_sel_hi:[1,0]
	v_pk_mul_f32 v[30:31], v[30:31], v[208:209] op_sel_hi:[1,0]
	v_pk_mul_f32 v[28:29], v[28:29], v[208:209] op_sel_hi:[1,0]
	v_pk_mul_f32 v[26:27], v[26:27], v[208:209] op_sel_hi:[1,0]
	v_pk_mul_f32 v[24:25], v[24:25], v[208:209] op_sel_hi:[1,0]
	v_pk_mul_f32 v[22:23], v[22:23], v[208:209] op_sel_hi:[1,0]
	v_pk_mul_f32 v[20:21], v[20:21], v[208:209] op_sel_hi:[1,0]
	v_pk_mul_f32 v[18:19], v[18:19], v[208:209] op_sel_hi:[1,0]
	v_pk_mul_f32 v[16:17], v[16:17], v[208:209] op_sel_hi:[1,0]
	v_pk_mul_f32 v[14:15], v[14:15], v[208:209] op_sel_hi:[1,0]
	v_pk_mul_f32 v[12:13], v[12:13], v[208:209] op_sel_hi:[1,0]
	v_pk_mul_f32 v[10:11], v[10:11], v[208:209] op_sel_hi:[1,0]
	v_pk_mul_f32 v[8:9], v[8:9], v[208:209] op_sel_hi:[1,0]
	v_pk_mul_f32 v[6:7], v[6:7], v[208:209] op_sel_hi:[1,0]
	v_pk_mul_f32 v[4:5], v[4:5], v[208:209] op_sel_hi:[1,0]
	v_pk_mul_f32 v[2:3], v[2:3], v[208:209] op_sel_hi:[1,0]
	v_mul_f32_e32 v205, v205, v208

.LBB0_476:
	s_nop 9
	v_max_f32_e32 v207, v82, v66
	v_max_f32_e32 v209, v83, v67
	v_max3_f32 v207, v207, s90, v209
	v_max_f32_e32 v209, v84, v68
	v_max_f32_e32 v210, v85, v69
	v_max3_f32 v207, v207, v209, v210
	v_max_f32_e32 v209, v86, v70
	v_max_f32_e32 v210, v87, v71
	v_max3_f32 v207, v207, v209, v210
	v_max_f32_e32 v209, v88, v72
	v_max_f32_e32 v210, v89, v73
	v_max3_f32 v207, v207, v209, v210
	v_max_f32_e32 v209, v90, v74
	v_max_f32_e32 v210, v91, v75
	v_max3_f32 v207, v207, v209, v210
	v_max_f32_e32 v209, v92, v76
	v_max_f32_e32 v210, v93, v77
	v_max3_f32 v207, v207, v209, v210
	v_max_f32_e32 v209, v94, v78
	v_max_f32_e32 v210, v95, v79
	v_max3_f32 v207, v207, v209, v210
	v_max_f32_e32 v209, v96, v80
	v_max_f32_e32 v210, v97, v81
	v_max3_f32 v207, v207, v209, v210
	v_mov_b32_e32 v209, v207
	v_mov_b32_e32 v210, v207
	s_nop 1
	v_permlane32_swap_b32_e32 v209, v210
	v_max3_f32 v207, v208, v209, v210
	v_cmp_neq_f32_e32 vcc, v207, v208
	s_cbranch_vccz .LBB0_478
	v_sub_f32_e32 v208, v208, v207
	v_mul_f32_e32 v208, 0x3dd53b94, v208
	v_exp_f32_e32 v208, v208
	s_nop 0
	v_pk_mul_f32 v[64:65], v[64:65], v[208:209] op_sel_hi:[1,0]
	v_pk_mul_f32 v[62:63], v[62:63], v[208:209] op_sel_hi:[1,0]
	v_pk_mul_f32 v[60:61], v[60:61], v[208:209] op_sel_hi:[1,0]
	v_pk_mul_f32 v[58:59], v[58:59], v[208:209] op_sel_hi:[1,0]
	v_pk_mul_f32 v[56:57], v[56:57], v[208:209] op_sel_hi:[1,0]
	v_pk_mul_f32 v[54:55], v[54:55], v[208:209] op_sel_hi:[1,0]
	v_pk_mul_f32 v[52:53], v[52:53], v[208:209] op_sel_hi:[1,0]
	v_pk_mul_f32 v[50:51], v[50:51], v[208:209] op_sel_hi:[1,0]
	v_pk_mul_f32 v[48:49], v[48:49], v[208:209] op_sel_hi:[1,0]
	v_pk_mul_f32 v[46:47], v[46:47], v[208:209] op_sel_hi:[1,0]
	v_pk_mul_f32 v[44:45], v[44:45], v[208:209] op_sel_hi:[1,0]
	v_pk_mul_f32 v[42:43], v[42:43], v[208:209] op_sel_hi:[1,0]
	v_pk_mul_f32 v[40:41], v[40:41], v[208:209] op_sel_hi:[1,0]
	v_pk_mul_f32 v[38:39], v[38:39], v[208:209] op_sel_hi:[1,0]
	v_pk_mul_f32 v[36:37], v[36:37], v[208:209] op_sel_hi:[1,0]
	v_pk_mul_f32 v[34:35], v[34:35], v[208:209] op_sel_hi:[1,0]
	v_pk_mul_f32 v[32:33], v[32:33], v[208:209] op_sel_hi:[1,0]
	v_pk_mul_f32 v[30:31], v[30:31], v[208:209] op_sel_hi:[1,0]
	v_pk_mul_f32 v[28:29], v[28:29], v[208:209] op_sel_hi:[1,0]
	v_pk_mul_f32 v[26:27], v[26:27], v[208:209] op_sel_hi:[1,0]
	v_pk_mul_f32 v[24:25], v[24:25], v[208:209] op_sel_hi:[1,0]
	v_pk_mul_f32 v[22:23], v[22:23], v[208:209] op_sel_hi:[1,0]
	v_pk_mul_f32 v[20:21], v[20:21], v[208:209] op_sel_hi:[1,0]
	v_pk_mul_f32 v[18:19], v[18:19], v[208:209] op_sel_hi:[1,0]
	v_pk_mul_f32 v[16:17], v[16:17], v[208:209] op_sel_hi:[1,0]
	v_pk_mul_f32 v[14:15], v[14:15], v[208:209] op_sel_hi:[1,0]
	v_pk_mul_f32 v[12:13], v[12:13], v[208:209] op_sel_hi:[1,0]
	v_pk_mul_f32 v[10:11], v[10:11], v[208:209] op_sel_hi:[1,0]
	v_pk_mul_f32 v[8:9], v[8:9], v[208:209] op_sel_hi:[1,0]
	v_pk_mul_f32 v[6:7], v[6:7], v[208:209] op_sel_hi:[1,0]
	v_pk_mul_f32 v[4:5], v[4:5], v[208:209] op_sel_hi:[1,0]
	v_pk_mul_f32 v[2:3], v[2:3], v[208:209] op_sel_hi:[1,0]
	v_mul_f32_e32 v205, v205, v208
